# attention: second unit of a workgroup reuses the upper 64 KiB of the w_uq LDS image (same head, other batch) instead of reloading it
# baseline (speedup 1.0000x reference)
; #define LAS __attribute__((address_space(3)))
; __device__ __forceinline__ void attn_unit(const unsigned char* __restrict__ CQt, const unsigned char* __restrict__ Wh, const f32x2* __restrict__ cst, const unsigned char* __restrict__ Kh, const unsigned char* __restrict__ Vh, bf16* __restrict__ Ob, char* lds) {
;     ...
;   {
; #pragma unroll
;     for (int i = 0; i < 12; ++i) { const int m = i * 512 + tid, row = m >> 5, cp = m & 31;
;       __builtin_amdgcn_global_load_lds((const unsigned*)(Wh + (long)row * QL + ((cp ^ (row & 15)) << 4)), (LAS unsigned*)(LAS char*)(lds + WIMG + (i * 8 + wid) * 1024), 16, 0, 0); }
;     ADMA(0, 0);
; __device__ __forceinline__ void attn_phase(CArgs& A, unsigned char* lds, int l) {
;     ...
;     for (int i = 0; i * G < NU; ++i) {
;         int L;
;         { const int x = c & 7, j = c >> 3; L = (i * 16 + x * 2 + (j >> 4)) * NQB + (j & 15); }
;         if (L >= NU) break;
;         const int bh = L / NQB, qb = L % NQB, b = bh / NH, h = bh % NH;
;         att::attn_unit(A.ws + WS_CQN + ((size_t)b * SEQ + qb * 256) * QL, A.ws + WS_WUQ + ((size_t)l * NH * DQK + (size_t)h * DQK) * QL, (const f32x2*)(A.ws + WS_CS) + ((size_t)b * SEQ + qb * 256) * 32, Kb + (size_t)bh * SEQ * DQK, Vb + (size_t)bh * SEQ * DV, FP8_WO ? (bf16*)((unsigned char*)(A.ws + WS_O8) + ((size_t)b * SEQ + qb * 256) * DM + h * DV) : O + ((size_t)b * SEQ + qb * 256) * DM + h * DV, (char*)lds);
.LBB0_879:
	s_add_i32 s9, s68, s2
	s_cmpk_gt_i32 s9, 0x1ff
	s_mov_b64 s[0:1], -1
	s_cbranch_scc1 .LBB0_878
	s_ashr_i32 s10, s9, 31
	s_lshr_b32 s0, s10, 28
	s_add_i32 s0, s9, s0
	s_ashr_i32 s12, s0, 4
	s_lshr_b32 s0, s12, 28
	v_mov_b32_e32 v189, v0
	s_add_i32 s0, s12, s0
	s_and_b32 s0, s0, -16
	v_readfirstlane_b32 s33, v189
	s_sub_i32 s63, s12, s0
	s_mul_i32 s0, s63, 0xc0
	v_mov_b32_e32 v2, s33
	v_bfi_b32 v2, s82, v2, v189
	v_mul_hi_i32 v3, v2, s83
	s_ashr_i32 s1, s0, 31
	v_lshrrev_b32_e32 v4, 31, v3
	v_ashrrev_i32_e32 v3, 1, v3
	s_lshl_b64 s[0:1], s[0:1], 9
	v_add_u32_e32 v3, v3, v4
	s_add_u32 s2, s75, s0
	v_mul_lo_u32 v4, v3, 12
	s_addc_u32 s3, s76, s1
	s_ashr_i32 s13, s12, 31
	s_mul_i32 s4, s12, 0xc0000
	v_sub_u32_e32 v4, v2, v4
	s_waitcnt lgkmcnt(0)
	v_lshrrev_b32_e32 v5, 2, v3
	s_mul_hi_i32 s5, s12, 0xc0000
	s_add_u32 s0, s69, s4
	v_bitop3_b32 v4, v5, v4, 3 bitop3:0x6c
	v_mul_lo_u32 v3, v3, s81
	s_addc_u32 s1, s70, s5
	v_lshl_add_u32 v164, v4, 4, v3
	s_ashr_i32 s14, s33, 6
	v_ashrrev_i32_e32 v4, 5, v189
	v_and_b32_e32 v170, 31, v189
	s_lshl_b32 s11, s14, 10
	v_ashrrev_i32_e32 v5, 31, v4
	s_add_i32 s86, s11, 0
	v_lshlrev_b64 v[6:7], 9, v[4:5]
	v_bitop3_b32 v3, v4, v170, 15 bitop3:0x6c
	s_add_i32 s88, s86, 0x8000
	v_lshl_add_u64 v[6:7], s[2:3], 0, v[6:7]
	v_lshlrev_b32_e32 v162, 4, v3
	v_lshl_add_u64 v[4:5], v[6:7], 0, v[162:163]
	s_mov_b32 m0, s88
	v_add_u32_e32 v3, 0x200, v189
	global_load_lds_dwordx4 v[4:5], off
	v_ashrrev_i32_e32 v4, 5, v3
	v_ashrrev_i32_e32 v5, 31, v4
	v_lshlrev_b64 v[6:7], 9, v[4:5]
	v_bitop3_b32 v3, v4, v170, 15 bitop3:0x6c
	v_lshl_add_u64 v[6:7], s[2:3], 0, v[6:7]
	v_lshlrev_b32_e32 v162, 4, v3
	s_add_i32 s89, s86, 0xa000
	v_lshl_add_u64 v[4:5], v[6:7], 0, v[162:163]
	s_mov_b32 m0, s89
	v_add_u32_e32 v3, 0x400, v189
	global_load_lds_dwordx4 v[4:5], off
	v_ashrrev_i32_e32 v4, 5, v3
	v_ashrrev_i32_e32 v5, 31, v4
	v_lshlrev_b64 v[6:7], 9, v[4:5]
	v_bitop3_b32 v3, v4, v170, 15 bitop3:0x6c
	v_lshl_add_u64 v[6:7], s[2:3], 0, v[6:7]
	v_lshlrev_b32_e32 v162, 4, v3
	s_add_i32 s90, s86, 0xc000
	v_lshl_add_u64 v[4:5], v[6:7], 0, v[162:163]
	s_mov_b32 m0, s90
	v_add_u32_e32 v3, 0x600, v189
	global_load_lds_dwordx4 v[4:5], off
	v_ashrrev_i32_e32 v4, 5, v3
	v_ashrrev_i32_e32 v5, 31, v4
	v_lshlrev_b64 v[6:7], 9, v[4:5]
	v_bitop3_b32 v3, v4, v170, 15 bitop3:0x6c
	v_lshl_add_u64 v[6:7], s[2:3], 0, v[6:7]
	v_lshlrev_b32_e32 v162, 4, v3
	s_add_i32 s91, s86, 0xe000
	v_lshl_add_u64 v[4:5], v[6:7], 0, v[162:163]
	s_mov_b32 m0, s91
	v_add_u32_e32 v3, 0x800, v189
	global_load_lds_dwordx4 v[4:5], off
	v_ashrrev_i32_e32 v4, 5, v3
	v_ashrrev_i32_e32 v5, 31, v4
	v_lshlrev_b64 v[6:7], 9, v[4:5]
	v_bitop3_b32 v3, v4, v170, 15 bitop3:0x6c
	v_lshl_add_u64 v[6:7], s[2:3], 0, v[6:7]
	v_lshlrev_b32_e32 v162, 4, v3
	v_lshl_add_u64 v[4:5], v[6:7], 0, v[162:163]
	s_add_i32 m0, s86, 0x10000
	v_add_u32_e32 v3, 0xa00, v189
	s_cmp_lg_u64 s[28:29], 0
	s_cbranch_scc1 .Limg_skip_1
	global_load_lds_dwordx4 v[4:5], off
.Limg_skip_1:
	v_ashrrev_i32_e32 v4, 5, v3
	v_ashrrev_i32_e32 v5, 31, v4
	v_lshlrev_b64 v[6:7], 9, v[4:5]
	v_bitop3_b32 v3, v4, v170, 15 bitop3:0x6c
	v_lshl_add_u64 v[6:7], s[2:3], 0, v[6:7]
	v_lshlrev_b32_e32 v162, 4, v3
	v_lshl_add_u64 v[4:5], v[6:7], 0, v[162:163]
	s_add_i32 m0, s86, 0x12000
	v_add_u32_e32 v3, 0xc00, v189
	s_cmp_lg_u64 s[28:29], 0
	s_cbranch_scc1 .Limg_skip_2
	global_load_lds_dwordx4 v[4:5], off
.Limg_skip_2:
	v_ashrrev_i32_e32 v4, 5, v3
	v_ashrrev_i32_e32 v5, 31, v4
	v_lshlrev_b64 v[6:7], 9, v[4:5]
	v_bitop3_b32 v3, v4, v170, 15 bitop3:0x6c
	v_lshl_add_u64 v[6:7], s[2:3], 0, v[6:7]
	v_lshlrev_b32_e32 v162, 4, v3
	v_lshl_add_u64 v[4:5], v[6:7], 0, v[162:163]
	s_add_i32 m0, s86, 0x14000
	v_add_u32_e32 v3, 0xe00, v189
	s_cmp_lg_u64 s[28:29], 0
	s_cbranch_scc1 .Limg_skip_3
	global_load_lds_dwordx4 v[4:5], off
.Limg_skip_3:
	v_ashrrev_i32_e32 v4, 5, v3
	v_ashrrev_i32_e32 v5, 31, v4
	v_lshlrev_b64 v[6:7], 9, v[4:5]
	v_bitop3_b32 v3, v4, v170, 15 bitop3:0x6c
	v_lshl_add_u64 v[6:7], s[2:3], 0, v[6:7]
	v_lshlrev_b32_e32 v162, 4, v3
	v_lshl_add_u64 v[4:5], v[6:7], 0, v[162:163]
	s_add_i32 m0, s86, 0x16000
	v_add_u32_e32 v3, 0x1000, v189
	s_cmp_lg_u64 s[28:29], 0
	s_cbranch_scc1 .Limg_skip_4
	global_load_lds_dwordx4 v[4:5], off
.Limg_skip_4:
	v_ashrrev_i32_e32 v4, 5, v3
	v_ashrrev_i32_e32 v5, 31, v4
	v_lshlrev_b64 v[6:7], 9, v[4:5]
	v_bitop3_b32 v3, v4, v170, 15 bitop3:0x6c
	v_lshl_add_u64 v[6:7], s[2:3], 0, v[6:7]
	v_lshlrev_b32_e32 v162, 4, v3
	v_lshl_add_u64 v[4:5], v[6:7], 0, v[162:163]
	s_add_i32 m0, s86, 0x18000
	v_add_u32_e32 v3, 0x1200, v189
	s_cmp_lg_u64 s[28:29], 0
	s_cbranch_scc1 .Limg_skip_5
	global_load_lds_dwordx4 v[4:5], off
.Limg_skip_5:
	v_ashrrev_i32_e32 v4, 5, v3
	v_ashrrev_i32_e32 v5, 31, v4
	v_lshlrev_b64 v[6:7], 9, v[4:5]
	v_bitop3_b32 v3, v4, v170, 15 bitop3:0x6c
	v_lshl_add_u64 v[6:7], s[2:3], 0, v[6:7]
	v_lshlrev_b32_e32 v162, 4, v3
	v_lshl_add_u64 v[4:5], v[6:7], 0, v[162:163]
	s_add_i32 m0, s86, 0x1a000
	v_add_u32_e32 v3, 0x1400, v189
	s_cmp_lg_u64 s[28:29], 0
	s_cbranch_scc1 .Limg_skip_6
	global_load_lds_dwordx4 v[4:5], off
.Limg_skip_6:
	v_ashrrev_i32_e32 v4, 5, v3
	v_ashrrev_i32_e32 v5, 31, v4
	v_lshlrev_b64 v[6:7], 9, v[4:5]
	v_bitop3_b32 v3, v4, v170, 15 bitop3:0x6c
	v_lshl_add_u64 v[6:7], s[2:3], 0, v[6:7]
	v_lshlrev_b32_e32 v162, 4, v3
	v_lshl_add_u64 v[4:5], v[6:7], 0, v[162:163]
	s_add_i32 m0, s86, 0x1c000
	v_add_u32_e32 v3, 0x1600, v189
	s_cmp_lg_u64 s[28:29], 0
	s_cbranch_scc1 .Limg_skip_7
	global_load_lds_dwordx4 v[4:5], off
.Limg_skip_7:
	v_ashrrev_i32_e32 v4, 5, v3
	v_ashrrev_i32_e32 v5, 31, v4
	v_lshlrev_b64 v[6:7], 9, v[4:5]
	v_bitop3_b32 v3, v4, v170, 15 bitop3:0x6c
	v_lshl_add_u64 v[6:7], s[2:3], 0, v[6:7]
	v_lshlrev_b32_e32 v162, 4, v3
	v_lshl_add_u64 v[4:5], v[6:7], 0, v[162:163]
	s_add_i32 m0, s86, 0x1e000
	v_ashrrev_i32_e32 v165, 31, v164
	s_add_i32 s87, s86, 0x2000
	s_cmp_lg_u64 s[28:29], 0
	s_cbranch_scc1 .Limg_skip_8
	global_load_lds_dwordx4 v[4:5], off
.Limg_skip_8:
	v_lshl_add_u64 v[4:5], s[0:1], 0, v[164:165]
	s_mov_b32 m0, s87
	v_add_u32_e32 v3, 0x200, v2
	global_load_lds_dwordx4 v[4:5], off
	v_mul_hi_i32 v4, v3, s83
	v_lshrrev_b32_e32 v5, 31, v4
	v_ashrrev_i32_e32 v4, 1, v4
	v_add_u32_e32 v4, v4, v5
	v_mul_lo_u32 v5, v4, 12
	v_sub_u32_e32 v3, v3, v5
	v_lshrrev_b32_e32 v5, 2, v4
	s_cmp_lt_i32 s14, 4
	v_bitop3_b32 v3, v5, v3, 3 bitop3:0x6c
	v_mul_lo_u32 v4, v4, s81
	s_cselect_b64 s[64:65], -1, 0
	s_cmp_gt_i32 s14, 3
	v_lshl_add_u32 v166, v3, 4, v4
	s_cselect_b64 s[2:3], -1, 0
	s_and_b64 vcc, exec, s[2:3]
	v_ashrrev_i32_e32 v167, 31, v166
	s_cbranch_vccnz .LBB0_882
	s_add_i32 m0, s86, 0x4000
	v_lshl_add_u64 v[4:5], s[0:1], 0, v[166:167]
	global_load_lds_dwordx4 v[4:5], off

; #define LAS __attribute__((address_space(3)))
; __device__ __forceinline__ void attn_unit(const unsigned char* __restrict__ CQt, const unsigned char* __restrict__ Wh, const f32x2* __restrict__ cst, const unsigned char* __restrict__ Kh, const unsigned char* __restrict__ Vh, bf16* __restrict__ Ob, char* lds) {
;     ...
;   {
; #pragma unroll
;     for (int i = 0; i < 12; ++i) { const int m = i * 512 + tid, row = m >> 5, cp = m & 31;
;       __builtin_amdgcn_global_load_lds((const unsigned*)(Wh + (long)row * QL + ((cp ^ (row & 15)) << 4)), (LAS unsigned*)(LAS char*)(lds + WIMG + (i * 8 + wid) * 1024), 16, 0, 0); }
;     ADMA(0, 0);
; __device__ __forceinline__ void attn_phase(CArgs& A, unsigned char* lds, int l) {
;     ...
;     for (int i = 0; i * G < NU; ++i) {
;         int L;
;         { const int x = c & 7, j = c >> 3; L = (i * 16 + x * 2 + (j >> 4)) * NQB + (j & 15); }
;         if (L >= NU) break;
;         const int bh = L / NQB, qb = L % NQB, b = bh / NH, h = bh % NH;
;         att::attn_unit(A.ws + WS_CQN + ((size_t)b * SEQ + qb * 256) * QL, A.ws + WS_WUQ + ((size_t)l * NH * DQK + (size_t)h * DQK) * QL, (const f32x2*)(A.ws + WS_CS) + ((size_t)b * SEQ + qb * 256) * 32, Kb + (size_t)bh * SEQ * DQK, Vb + (size_t)bh * SEQ * DV, FP8_WO ? (bf16*)((unsigned char*)(A.ws + WS_O8) + ((size_t)b * SEQ + qb * 256) * DM + h * DV) : O + ((size_t)b * SEQ + qb * 256) * DM + h * DV, (char*)lds);
.LBB0_2142:
	s_add_i32 s10, s68, s2
	s_cmpk_gt_i32 s10, 0x1ff
	s_mov_b64 s[0:1], -1
	s_cbranch_scc1 .LBB0_2141
	s_ashr_i32 s11, s10, 31
	s_lshr_b32 s0, s11, 28
	s_add_i32 s0, s10, s0
	s_ashr_i32 s12, s0, 4
	s_lshr_b32 s0, s12, 28
	v_mov_b32_e32 v189, v0
	s_add_i32 s0, s12, s0
	s_and_b32 s0, s0, -16
	v_readfirstlane_b32 s33, v189
	s_sub_i32 s63, s12, s0
	s_mul_i32 s0, s63, 0xc0
	v_mov_b32_e32 v2, s33
	v_bfi_b32 v2, s82, v2, v189
	v_mul_hi_i32 v3, v2, s83
	s_add_i32 s8, s0, 0xc00
	v_lshrrev_b32_e32 v4, 31, v3
	v_ashrrev_i32_e32 v3, 1, v3
	s_lshl_b64 s[0:1], s[8:9], 9
	v_add_u32_e32 v3, v3, v4
	s_add_u32 s2, s75, s0
	v_mul_lo_u32 v4, v3, 12
	s_addc_u32 s3, s76, s1
	s_ashr_i32 s13, s12, 31
	s_mul_i32 s4, s12, 0xc0000
	v_sub_u32_e32 v4, v2, v4
	s_waitcnt lgkmcnt(0)
	v_lshrrev_b32_e32 v5, 2, v3
	s_mul_hi_i32 s5, s12, 0xc0000
	s_add_u32 s0, s69, s4
	v_bitop3_b32 v4, v5, v4, 3 bitop3:0x6c
	v_mul_lo_u32 v3, v3, s81
	s_addc_u32 s1, s70, s5
	v_lshl_add_u32 v164, v4, 4, v3
	s_ashr_i32 s8, s33, 6
	v_ashrrev_i32_e32 v4, 5, v189
	v_and_b32_e32 v170, 31, v189
	s_lshl_b32 s14, s8, 10
	v_ashrrev_i32_e32 v5, 31, v4
	s_add_i32 s86, s14, 0
	v_lshlrev_b64 v[6:7], 9, v[4:5]
	v_bitop3_b32 v3, v4, v170, 15 bitop3:0x6c
	s_add_i32 s88, s86, 0x8000
	v_lshl_add_u64 v[6:7], s[2:3], 0, v[6:7]
	v_lshlrev_b32_e32 v162, 4, v3
	v_lshl_add_u64 v[4:5], v[6:7], 0, v[162:163]
	s_mov_b32 m0, s88
	v_add_u32_e32 v3, 0x200, v189
	global_load_lds_dwordx4 v[4:5], off
	v_ashrrev_i32_e32 v4, 5, v3
	v_ashrrev_i32_e32 v5, 31, v4
	v_lshlrev_b64 v[6:7], 9, v[4:5]
	v_bitop3_b32 v3, v4, v170, 15 bitop3:0x6c
	v_lshl_add_u64 v[6:7], s[2:3], 0, v[6:7]
	v_lshlrev_b32_e32 v162, 4, v3
	s_add_i32 s89, s86, 0xa000
	v_lshl_add_u64 v[4:5], v[6:7], 0, v[162:163]
	s_mov_b32 m0, s89
	v_add_u32_e32 v3, 0x400, v189
	global_load_lds_dwordx4 v[4:5], off
	v_ashrrev_i32_e32 v4, 5, v3
	v_ashrrev_i32_e32 v5, 31, v4
	v_lshlrev_b64 v[6:7], 9, v[4:5]
	v_bitop3_b32 v3, v4, v170, 15 bitop3:0x6c
	v_lshl_add_u64 v[6:7], s[2:3], 0, v[6:7]
	v_lshlrev_b32_e32 v162, 4, v3
	s_add_i32 s90, s86, 0xc000
	v_lshl_add_u64 v[4:5], v[6:7], 0, v[162:163]
	s_mov_b32 m0, s90
	v_add_u32_e32 v3, 0x600, v189
	global_load_lds_dwordx4 v[4:5], off
	v_ashrrev_i32_e32 v4, 5, v3
	v_ashrrev_i32_e32 v5, 31, v4
	v_lshlrev_b64 v[6:7], 9, v[4:5]
	v_bitop3_b32 v3, v4, v170, 15 bitop3:0x6c
	v_lshl_add_u64 v[6:7], s[2:3], 0, v[6:7]
	v_lshlrev_b32_e32 v162, 4, v3
	s_add_i32 s91, s86, 0xe000
	v_lshl_add_u64 v[4:5], v[6:7], 0, v[162:163]
	s_mov_b32 m0, s91
	v_add_u32_e32 v3, 0x800, v189
	global_load_lds_dwordx4 v[4:5], off
	v_ashrrev_i32_e32 v4, 5, v3
	v_ashrrev_i32_e32 v5, 31, v4
	v_lshlrev_b64 v[6:7], 9, v[4:5]
	v_bitop3_b32 v3, v4, v170, 15 bitop3:0x6c
	v_lshl_add_u64 v[6:7], s[2:3], 0, v[6:7]
	v_lshlrev_b32_e32 v162, 4, v3
	v_lshl_add_u64 v[4:5], v[6:7], 0, v[162:163]
	s_add_i32 m0, s86, 0x10000
	v_add_u32_e32 v3, 0xa00, v189
	s_cmp_lg_u64 s[28:29], 0
	s_cbranch_scc1 .Limg_skip_9
	global_load_lds_dwordx4 v[4:5], off

; #define LAS __attribute__((address_space(3)))
; __device__ __forceinline__ void attn_unit(const unsigned char* __restrict__ CQt, const unsigned char* __restrict__ Wh, const f32x2* __restrict__ cst, const unsigned char* __restrict__ Kh, const unsigned char* __restrict__ Vh, bf16* __restrict__ Ob, char* lds) {
;     ...
;       __builtin_amdgcn_global_load_lds((const unsigned*)(Wh + (long)row * QL + ((cp ^ (row & 15)) << 4)), (LAS unsigned*)(LAS char*)(lds + WIMG + (i * 8 + wid) * 1024), 16, 0, 0); }
;     ADMA(0, 0);
.Limg_skip_16:
	v_lshl_add_u64 v[4:5], s[0:1], 0, v[164:165]
	s_mov_b32 m0, s87
	v_add_u32_e32 v3, 0x200, v2
	global_load_lds_dwordx4 v[4:5], off
	v_mul_hi_i32 v4, v3, s83
	v_lshrrev_b32_e32 v5, 31, v4
	v_ashrrev_i32_e32 v4, 1, v4
	v_add_u32_e32 v4, v4, v5
	v_mul_lo_u32 v5, v4, 12
	v_sub_u32_e32 v3, v3, v5
	v_lshrrev_b32_e32 v5, 2, v4
	s_cmp_lt_i32 s8, 4
	v_bitop3_b32 v3, v5, v3, 3 bitop3:0x6c
	v_mul_lo_u32 v4, v4, s81
	s_cselect_b64 s[64:65], -1, 0
	s_cmp_gt_i32 s8, 3
	v_lshl_add_u32 v166, v3, 4, v4
	s_cselect_b64 s[2:3], -1, 0
	s_and_b64 vcc, exec, s[2:3]
	v_ashrrev_i32_e32 v167, 31, v166
	s_cbranch_vccnz .LBB0_2145
	s_add_i32 m0, s86, 0x4000
	v_lshl_add_u64 v[4:5], s[0:1], 0, v[166:167]
	global_load_lds_dwordx4 v[4:5], off
